# SWA L0 QK K-fragment LDS reads batched up front with counted lgkmcnt waits
# speedup vs baseline: 1.0104x; 1.0018x over previous
; #define LAS __attribute__((address_space(3)))
; __device__ __forceinline__ float xhalf_max(float v) { auto rr = __builtin_amdgcn_permlane32_swap(__float_as_uint(v), __float_as_uint(v), false, false); return fmaxf(__uint_as_float(rr[0]), __uint_as_float(rr[1])); }
; template <int MODE>
; __device__ __forceinline__ void tile(LAS unsigned char* lds, int kt, const bf16x8 (&qf)[4], State& st, int lane) {
;     const int r32 = lane & 31, h = lane >> 5;
;     f32x16 S;
;     if (MODE == 3) S = st.negm;
;     else {
; #pragma unroll
;         for (int r = 0; r < 16; ++r) { const int ko = (r & 3) + 8 * (r >> 2) + 4 * h; const bool ok = (MODE == 1) ? (ko <= r32) : (ko > r32); S[r] = ok ? st.negm[r] : NEG; } }
;     const LAS unsigned char* kp = lds + K_OFF + (kt * 32 + r32) * KROW + h * 16;
; #pragma unroll
;     for (int s = 0; s < 4; ++s) { const bf16x8 a = *(const LAS bf16x8*)(kp + s * 32); S = __builtin_amdgcn_mfma_f32_32x32x16_bf16(a, qf[s], S, 0, 0, 0); }
;     float tmax;
;     asm volatile("s_nop 15\n\ts_nop 7" : "+v"(S));
;     { float m0, m1, m2, m3, m4;
;       asm("v_max3_f32 %0, %1, %2, %3" : "=v"(m0) : "v"(S[0]), "v"(S[1]), "v"(S[2]));    asm("v_max3_f32 %0, %1, %2, %3" : "=v"(m1) : "v"(S[3]), "v"(S[4]), "v"(S[5]));
;       asm("v_max3_f32 %0, %1, %2, %3" : "=v"(m2) : "v"(S[6]), "v"(S[7]), "v"(S[8]));    asm("v_max3_f32 %0, %1, %2, %3" : "=v"(m3) : "v"(S[9]), "v"(S[10]), "v"(S[11]));
;       asm("v_max3_f32 %0, %1, %2, %3" : "=v"(m4) : "v"(S[12]), "v"(S[13]), "v"(S[14])); asm("v_max3_f32 %0, %1, %2, %3" : "=v"(m0) : "v"(m0), "v"(m1), "v"(S[15]));
;       asm("v_max3_f32 %0, %1, %2, %3" : "=v"(m2) : "v"(m2), "v"(m3), "v"(m4));          asm("v_max_f32 %0, %1, %2" : "=v"(tmax) : "v"(m0), "v"(m2)); }
;     tmax = xhalf_max(tmax);
;     if (__any(tmax > THR)) {
;         const float d = tmax > THR ? tmax : 0.f, alpha = __builtin_amdgcn_exp2f(-d);
;         st.m += d; st.l *= alpha;
; #pragma unroll
;         for (int r = 0; r < 16; ++r) { S[r] -= d; st.negm[r] -= d; st.o0[r] *= alpha; st.o1[r] *= alpha; }
;     }
.LBB0_909:
	s_andn2_b64 vcc, exec, s[52:53]
	s_cbranch_vccnz .LBB0_912
	v_or_b32_e32 v1, s72, v139
	v_mad_u64_u32 v[8:9], s[52:53], v1, s55, v[142:143]
	ds_read_b128 v[4:7], v8
	ds_read_b128 v[164:167], v8 offset:32
	ds_read_b128 v[168:171], v8 offset:64
	ds_read_b128 v[172:175], v8 offset:96
	s_waitcnt vmcnt(1) lgkmcnt(3)
	v_mfma_f32_32x32x16_bf16 v[66:81], v[4:7], v[126:129], v[34:49]
	s_waitcnt lgkmcnt(2)
	v_mfma_f32_32x32x16_bf16 v[66:81], v[164:167], v[122:125], v[66:81]
	s_waitcnt lgkmcnt(1)
	v_mfma_f32_32x32x16_bf16 v[66:81], v[168:171], v[118:121], v[66:81]
	s_waitcnt vmcnt(0) lgkmcnt(0)
	v_mfma_f32_32x32x16_bf16 v[66:81], v[172:175], v[114:117], v[66:81]
	s_nop 15
	s_nop 7
	s_nop 0
	v_max3_f32 v1, v66, v67, v68
	v_max3_f32 v3, v69, v70, v71
	v_max3_f32 v4, v72, v73, v74
	v_max3_f32 v5, v75, v76, v77
	v_max3_f32 v6, v78, v79, v80
	s_nop 0
	v_max3_f32 v1, v1, v3, v81
	v_max3_f32 v3, v4, v5, v6
	s_nop 0
	v_max_f32 v1, v1, v3
	s_nop 0
	v_mov_b32_e32 v3, v1
	s_nop 1
	v_permlane32_swap_b32_e32 v1, v3
	v_max_f32_e32 v3, v3, v3
	v_max_f32_e32 v1, v1, v1
	v_max_f32_e32 v1, v1, v3
	v_cmp_lt_f32_e32 vcc, s63, v1
	s_cbranch_vccz .LBB0_913
	s_nop 0
	v_cndmask_b32_e32 v4, 0, v1, vcc
	v_exp_f32_e64 v3, -v4
	v_sub_f32_e32 v82, 0x447a0000, v4
	v_add_f32_e32 v1, 0xc47a0000, v4
	v_pk_add_f32 v[66:67], v[66:67], v[4:5] op_sel_hi:[1,0] neg_lo:[0,1] neg_hi:[0,1]
	v_mul_f32_e32 v50, 0, v3
	v_pk_add_f32 v[68:69], v[68:69], v[4:5] op_sel_hi:[1,0] neg_lo:[0,1] neg_hi:[0,1]
	v_pk_add_f32 v[70:71], v[70:71], v[4:5] op_sel_hi:[1,0] neg_lo:[0,1] neg_hi:[0,1]
	v_pk_add_f32 v[72:73], v[72:73], v[4:5] op_sel_hi:[1,0] neg_lo:[0,1] neg_hi:[0,1]
	v_pk_add_f32 v[74:75], v[74:75], v[4:5] op_sel_hi:[1,0] neg_lo:[0,1] neg_hi:[0,1]
	v_pk_add_f32 v[76:77], v[76:77], v[4:5] op_sel_hi:[1,0] neg_lo:[0,1] neg_hi:[0,1]
	v_pk_add_f32 v[78:79], v[78:79], v[4:5] op_sel_hi:[1,0] neg_lo:[0,1] neg_hi:[0,1]
	v_pk_add_f32 v[80:81], v[80:81], v[4:5] op_sel_hi:[1,0] neg_lo:[0,1] neg_hi:[0,1]
	v_mov_b32_e32 v83, v82
	v_mov_b32_e32 v84, v82
	v_mov_b32_e32 v85, v82
	v_mov_b32_e32 v86, v82
	v_mov_b32_e32 v87, v82
	v_mov_b32_e32 v88, v82
	v_mov_b32_e32 v89, v82
	v_mov_b32_e32 v90, v82
	v_mov_b32_e32 v91, v82
	v_mov_b32_e32 v92, v82
	v_mov_b32_e32 v93, v82
	v_mov_b32_e32 v94, v82
	v_mov_b32_e32 v95, v82
	v_mov_b32_e32 v96, v82
	v_mov_b32_e32 v97, v82
	s_branch .LBB0_914

; #define LAS __attribute__((address_space(3)))
; __device__ __forceinline__ float xhalf_max(float v) { auto rr = __builtin_amdgcn_permlane32_swap(__float_as_uint(v), __float_as_uint(v), false, false); return fmaxf(__uint_as_float(rr[0]), __uint_as_float(rr[1])); }
; template <int MODE>
; __device__ __forceinline__ void tile(LAS unsigned char* lds, int kt, const bf16x8 (&qf)[4], State& st, int lane) {
;     const int r32 = lane & 31, h = lane >> 5;
;     f32x16 S;
;     if (MODE == 3) S = st.negm;
;     else {
; #pragma unroll
;         for (int r = 0; r < 16; ++r) { const int ko = (r & 3) + 8 * (r >> 2) + 4 * h; const bool ok = (MODE == 1) ? (ko <= r32) : (ko > r32); S[r] = ok ? st.negm[r] : NEG; } }
;     const LAS unsigned char* kp = lds + K_OFF + (kt * 32 + r32) * KROW + h * 16;
; #pragma unroll
;     for (int s = 0; s < 4; ++s) { const bf16x8 a = *(const LAS bf16x8*)(kp + s * 32); S = __builtin_amdgcn_mfma_f32_32x32x16_bf16(a, qf[s], S, 0, 0, 0); }
;     float tmax;
;     asm volatile("s_nop 15\n\ts_nop 7" : "+v"(S));
;     { float m0, m1, m2, m3, m4;
;       asm("v_max3_f32 %0, %1, %2, %3" : "=v"(m0) : "v"(S[0]), "v"(S[1]), "v"(S[2]));    asm("v_max3_f32 %0, %1, %2, %3" : "=v"(m1) : "v"(S[3]), "v"(S[4]), "v"(S[5]));
;       asm("v_max3_f32 %0, %1, %2, %3" : "=v"(m2) : "v"(S[6]), "v"(S[7]), "v"(S[8]));    asm("v_max3_f32 %0, %1, %2, %3" : "=v"(m3) : "v"(S[9]), "v"(S[10]), "v"(S[11]));
;       asm("v_max3_f32 %0, %1, %2, %3" : "=v"(m4) : "v"(S[12]), "v"(S[13]), "v"(S[14])); asm("v_max3_f32 %0, %1, %2, %3" : "=v"(m0) : "v"(m0), "v"(m1), "v"(S[15]));
;       asm("v_max3_f32 %0, %1, %2, %3" : "=v"(m2) : "v"(m2), "v"(m3), "v"(m4));          asm("v_max_f32 %0, %1, %2" : "=v"(tmax) : "v"(m0), "v"(m2)); }
;     tmax = xhalf_max(tmax);
;     if (__any(tmax > THR)) {
;         const float d = tmax > THR ? tmax : 0.f, alpha = __builtin_amdgcn_exp2f(-d);
;         st.m += d; st.l *= alpha;
; #pragma unroll
;         for (int r = 0; r < 16; ++r) { S[r] -= d; st.negm[r] -= d; st.o0[r] *= alpha; st.o1[r] *= alpha; }
;     }
.LBB0_918:
	ds_read_b128 v[6:9], v4
	ds_read_b128 v[164:167], v4 offset:32
	ds_read_b128 v[168:171], v4 offset:64
	ds_read_b128 v[172:175], v4 offset:96
	s_waitcnt vmcnt(1) lgkmcnt(3)
	v_mfma_f32_32x32x16_bf16 v[98:113], v[6:9], v[126:129], v[82:97]
	s_waitcnt lgkmcnt(2)
	v_mfma_f32_32x32x16_bf16 v[98:113], v[164:167], v[122:125], v[98:113]
	s_waitcnt lgkmcnt(1)
	v_mfma_f32_32x32x16_bf16 v[98:113], v[168:171], v[118:121], v[98:113]
	s_waitcnt vmcnt(0) lgkmcnt(0)
	v_mfma_f32_32x32x16_bf16 v[98:113], v[172:175], v[114:117], v[98:113]
	s_nop 15
	s_nop 7
	s_nop 0
	v_max3_f32 v5, v98, v99, v100
	v_max3_f32 v6, v101, v102, v103
	v_max3_f32 v7, v104, v105, v106
	v_max3_f32 v8, v107, v108, v109
	v_max3_f32 v9, v110, v111, v112
	s_nop 0
	v_max3_f32 v5, v5, v6, v113
	v_max3_f32 v6, v7, v8, v9
	s_nop 0
	v_max_f32 v5, v5, v6
	s_nop 0
	v_mov_b32_e32 v6, v5
	s_nop 1
	v_permlane32_swap_b32_e32 v5, v6
	v_max_f32_e32 v6, v6, v6
	v_max_f32_e32 v5, v5, v5
	v_max_f32_e32 v5, v5, v6
	v_cmp_lt_f32_e32 vcc, s63, v5
	s_cbranch_vccz .LBB0_917
	s_nop 0
	v_cndmask_b32_e32 v6, 0, v5, vcc
	v_exp_f32_e64 v8, -v6
	v_add_f32_e32 v1, v1, v6
	v_pk_add_f32 v[98:99], v[98:99], v[6:7] op_sel_hi:[1,0] neg_lo:[0,1] neg_hi:[0,1]
	v_pk_add_f32 v[100:101], v[100:101], v[6:7] op_sel_hi:[1,0] neg_lo:[0,1] neg_hi:[0,1]
	v_mul_f32_e32 v160, v160, v8
	v_pk_add_f32 v[102:103], v[102:103], v[6:7] op_sel_hi:[1,0] neg_lo:[0,1] neg_hi:[0,1]
	v_pk_add_f32 v[104:105], v[104:105], v[6:7] op_sel_hi:[1,0] neg_lo:[0,1] neg_hi:[0,1]
	v_pk_add_f32 v[106:107], v[106:107], v[6:7] op_sel_hi:[1,0] neg_lo:[0,1] neg_hi:[0,1]
	v_pk_add_f32 v[108:109], v[108:109], v[6:7] op_sel_hi:[1,0] neg_lo:[0,1] neg_hi:[0,1]
	v_pk_add_f32 v[110:111], v[110:111], v[6:7] op_sel_hi:[1,0] neg_lo:[0,1] neg_hi:[0,1]
	v_pk_add_f32 v[112:113], v[112:113], v[6:7] op_sel_hi:[1,0] neg_lo:[0,1] neg_hi:[0,1]
	v_sub_f32_e32 v97, v97, v6
	v_sub_f32_e32 v96, v96, v6
	v_sub_f32_e32 v95, v95, v6
	v_sub_f32_e32 v94, v94, v6
	v_sub_f32_e32 v93, v93, v6
	v_sub_f32_e32 v92, v92, v6
	v_sub_f32_e32 v91, v91, v6
	v_sub_f32_e32 v90, v90, v6
	v_sub_f32_e32 v89, v89, v6
	v_sub_f32_e32 v88, v88, v6
	v_sub_f32_e32 v87, v87, v6
	v_sub_f32_e32 v86, v86, v6
	v_sub_f32_e32 v85, v85, v6
	v_sub_f32_e32 v84, v84, v6
	v_sub_f32_e32 v83, v83, v6
	v_sub_f32_e32 v82, v82, v6
	v_pk_mul_f32 v[80:81], v[80:81], v[8:9] op_sel_hi:[1,0]
	v_pk_mul_f32 v[78:79], v[78:79], v[8:9] op_sel_hi:[1,0]
	v_pk_mul_f32 v[76:77], v[76:77], v[8:9] op_sel_hi:[1,0]
	v_pk_mul_f32 v[74:75], v[74:75], v[8:9] op_sel_hi:[1,0]
	v_pk_mul_f32 v[72:73], v[72:73], v[8:9] op_sel_hi:[1,0]
	v_pk_mul_f32 v[70:71], v[70:71], v[8:9] op_sel_hi:[1,0]
	v_pk_mul_f32 v[68:69], v[68:69], v[8:9] op_sel_hi:[1,0]
	v_pk_mul_f32 v[66:67], v[66:67], v[8:9] op_sel_hi:[1,0]
	v_pk_mul_f32 v[64:65], v[64:65], v[8:9] op_sel_hi:[1,0]
	v_pk_mul_f32 v[62:63], v[62:63], v[8:9] op_sel_hi:[1,0]
	v_pk_mul_f32 v[60:61], v[60:61], v[8:9] op_sel_hi:[1,0]
	v_pk_mul_f32 v[58:59], v[58:59], v[8:9] op_sel_hi:[1,0]
	v_pk_mul_f32 v[56:57], v[56:57], v[8:9] op_sel_hi:[1,0]
	v_pk_mul_f32 v[54:55], v[54:55], v[8:9] op_sel_hi:[1,0]
	v_pk_mul_f32 v[52:53], v[52:53], v[8:9] op_sel_hi:[1,0]
	v_pk_mul_f32 v[50:51], v[50:51], v[8:9] op_sel_hi:[1,0]
	s_branch .LBB0_917
